# retention scan units: per-head log-decay constants from an 8-entry table instead of two log1pf expansions per unit (450 dead instructions removed)
# baseline (speedup 1.0000x reference)
; DEVI bf16_t f2bf(float x) { return (bf16_t)(cvt_pk(x, 0.f) & 0xffffu); }
; DEVI int opaque_tid() { int t = threadIdx.x; asm volatile("" : "+v"(t)); return t; }
; DEVI void ret_decays(int h, float& ldf, float& ldb) { ldf = log1pf(-exp2f(-(5.f + 2.f * h))); ldb = log1pf(-exp2f(-(6.f + 2.f * h))); }
; DEVI void scan_a_ret(const Params& p, int l, int b, int h, int c, const RetIn& in, char* smem) {
;     bf16_t* kTf = (bf16_t*)smem; bf16_t* kTb = kTf + 128 * 72; bf16_t* vT = kTb + 128 * 72;
;     const int tid = opaque_tid(), wid = tid >> 6, lane = tid & 63, fr = lane & 15, fq = lane >> 4;
;     const bool lat = c >= 4;
;     const int tk = tid >> 3, kk16 = (tid & 7) * 16;
;     float ldf, ldb; ret_decays(h, ldf, ldb);
;     float kf[16];
;     ret_rot(in.k0, in.k1, in, lat, 0.08838834764831845f, kf);
;     const float ef = __expf(ldf * (float)(63 - tk)), eb = __expf(ldb * (float)tk);
; #pragma unroll
;     for (int e = 0; e < 16; ++e) { kTf[(kk16 + e) * 72 + tk] = f2bf(kf[e] * ef); kTb[(kk16 + e) * 72 + tk] = f2bf(kf[e] * eb); }
;     {   const bf16x8 v0 = in.v0, v1 = in.v1;
; #pragma unroll
;         for (int e = 0; e < 8; ++e) { vT[(kk16 + e) * 72 + tk] = (bf16_t)v0[e]; vT[(kk16 + 8 + e) * 72 + tk] = (bf16_t)v1[e]; } }
;     __syncthreads();
;     {   const int dir = wid >> 2;
;         const bf16_t* kT = dir ? kTb : kTf;
;         bf16_t* UT = (bf16_t*)(p.ws + WS_UTR) + ((size_t)((b * 4 + h) * 2 + dir) * NCH + order_idx(dir, c)) * (128 * 128);
.LBB0_531:
	s_lshl_b32 s6, s6, 1
	s_and_b32 s7, s6, 6
	v_mov_b32_e32 v214, 0xbc8102b3
	v_mov_b32_e32 v216, 0xbb80402b
	v_cmp_eq_u32_e64 vcc, s7, 2
	v_cndmask_b32_e32 v214, v214, v216, vcc
	v_mov_b32_e32 v216, 0xba801003
	v_cmp_eq_u32_e64 vcc, s7, 4
	v_cndmask_b32_e32 v214, v214, v216, vcc
	v_mov_b32_e32 v216, 0xb9800400
	v_cmp_eq_u32_e64 vcc, s7, 6
	v_cndmask_b32_e32 v214, v214, v216, vcc
	v_mov_b32_e32 v215, 0xbd020aec
	v_mov_b32_e32 v216, 0xbc0080ac
	v_cmp_eq_u32_e64 vcc, s7, 2
	v_cndmask_b32_e32 v215, v215, v216, vcc
	v_mov_b32_e32 v216, 0xbb00200b
	v_cmp_eq_u32_e64 vcc, s7, 4
	v_cndmask_b32_e32 v215, v215, v216, vcc
	v_mov_b32_e32 v216, 0xba000801
	v_cmp_eq_u32_e64 vcc, s7, 6
	v_cndmask_b32_e32 v215, v215, v216, vcc
	s_mov_b32 s25, 0x42fc0000
	s_mov_b32 s29, 0x3f2aaaab
	s_mov_b32 s33, 0x3f317218
	s_mov_b32 s28, 0x33800000
	s_add_i32 s7, s7, 5
	v_mul_f32_e32 v84, 0x3db504f3, v84
	v_mul_f32_e32 v85, 0x3db504f3, v85
	v_mov_b32_e32 v1, v214
	v_cvt_f32_ubyte0_e32 v2, s7
	v_cmp_lt_f32_e32 vcc, s25, v2
	s_and_b64 s[16:17], vcc, exec
	s_cselect_b32 s7, 0xffffffc0, 0
	v_cndmask_b32_e32 v78, 0, v226, vcc
	v_sub_f32_e32 v2, v78, v2
	v_exp_f32_e32 v2, v2
	v_mul_f32_e32 v86, 0x3db504f3, v86
	v_mul_f32_e32 v87, 0x3db504f3, v87
	v_mul_f32_e32 v80, 0x3db504f3, v80
	v_ldexp_f32 v2, v2, s7
	v_ashrrev_i32_e32 v79, 3, v124
	v_sub_u32_e32 v96, 63, v79
	v_cvt_f32_i32_e32 v96, v96
	v_cmp_gt_f32_e32 vcc, s28, v2
	v_cmp_neq_f32_e64 s[38:39], 1.0, v2
	v_mul_f32_e32 v83, 0x3db504f3, v107
	s_movk_i32 s7, 0x48
	v_mov_b32_e32 v2, v215
	v_mul_f32_e32 v2, v2, v96
	v_cvt_f32_i32_e32 v96, v79
	v_mul_f32_e32 v2, 0x3fb8aa3b, v2
	v_exp_f32_e32 v2, v2
	v_lshlrev_b32_e32 v78, 4, v124
	v_mul_f32_e32 v1, v1, v96
	v_mul_f32_e32 v1, 0x3fb8aa3b, v1
	v_exp_f32_e32 v1, v1
	v_and_b32_e32 v78, 0x70, v78
	v_mul_f32_e32 v96, v2, v83
	v_mul_u32_u24_e32 v97, 0x48, v78
	v_mad_u32_u24 v78, v78, s7, v79
	v_mul_f32_e32 v83, v1, v83
	v_lshl_add_u32 v78, v78, 1, 0
	v_cvt_pk_bf16_f32 v83, v83, s0
	ds_write_b16 v78, v83 offset:18432
	v_mul_f32_e32 v83, v2, v84
	v_cvt_pk_bf16_f32 v83, v83, s0
	ds_write_b16 v78, v83 offset:144
	v_mul_f32_e32 v83, v1, v84
	v_mul_f32_e32 v89, 0x3db504f3, v106
	v_cvt_pk_bf16_f32 v83, v83, s0
	ds_write_b16 v78, v83 offset:18576
	v_mul_f32_e32 v83, v2, v89
	v_cvt_pk_bf16_f32 v83, v83, s0
	ds_write_b16 v78, v83 offset:288
	v_mul_f32_e32 v83, v1, v89
	v_cvt_pk_bf16_f32 v83, v83, s0
	ds_write_b16 v78, v83 offset:18720
	v_mul_f32_e32 v83, v2, v85
	v_cvt_pk_bf16_f32 v83, v83, s0
	ds_write_b16 v78, v83 offset:432
	v_mul_f32_e32 v83, v1, v85
	v_mul_f32_e32 v90, 0x3db504f3, v105
	v_cvt_pk_bf16_f32 v83, v83, s0
	ds_write_b16 v78, v83 offset:18864
	v_mul_f32_e32 v83, v2, v90
	v_cvt_pk_bf16_f32 v83, v83, s0
	ds_write_b16 v78, v83 offset:576
	v_mul_f32_e32 v83, v1, v90
	v_cvt_pk_bf16_f32 v83, v83, s0
	ds_write_b16 v78, v83 offset:19008
	v_mul_f32_e32 v83, v2, v86
	v_cvt_pk_bf16_f32 v83, v83, s0
	ds_write_b16 v78, v83 offset:720
	v_mul_f32_e32 v83, v1, v86
	v_mul_f32_e32 v91, 0x3db504f3, v104
	v_cvt_pk_bf16_f32 v83, v83, s0
	ds_write_b16 v78, v83 offset:19152
	v_mul_f32_e32 v83, v2, v91
	v_cvt_pk_bf16_f32 v83, v83, s0
	ds_write_b16 v78, v83 offset:864
	v_mul_f32_e32 v83, v1, v91
	v_cvt_pk_bf16_f32 v83, v83, s0
	ds_write_b16 v78, v83 offset:19296
	v_mul_f32_e32 v83, v2, v87
	v_cvt_pk_bf16_f32 v83, v83, s0
	ds_write_b16 v78, v83 offset:1008
	v_mul_f32_e32 v83, v1, v87
	v_mul_f32_e32 v92, 0x3db504f3, v103
	v_cvt_pk_bf16_f32 v83, v83, s0
	ds_write_b16 v78, v83 offset:19440
	v_mul_f32_e32 v83, v2, v92
	v_cvt_pk_bf16_f32 v83, v83, s0
	ds_write_b16 v78, v83 offset:1152
	v_mul_f32_e32 v83, v1, v92
	v_cvt_pk_bf16_f32 v83, v83, s0
	ds_write_b16 v78, v83 offset:19584
	v_mul_f32_e32 v83, v2, v80
	v_mul_f32_e32 v80, v1, v80
	v_mul_f32_e32 v93, 0x3db504f3, v102
	v_cvt_pk_bf16_f32 v80, v80, s0
	ds_write_b16 v78, v80 offset:19728
	v_mul_f32_e32 v80, v2, v93
	v_cvt_pk_bf16_f32 v80, v80, s0
	ds_write_b16 v78, v80 offset:1440
	v_mul_f32_e32 v80, v1, v93
	v_mul_f32_e32 v81, 0x3db504f3, v81
	v_cvt_pk_bf16_f32 v80, v80, s0
	ds_write_b16 v78, v80 offset:19872
	v_mul_f32_e32 v80, v2, v81
	v_cvt_pk_bf16_f32 v80, v80, s0
	ds_write_b16 v78, v80 offset:1584
	v_mul_f32_e32 v80, v1, v81
	v_mul_f32_e32 v94, 0x3db504f3, v101
	v_cvt_pk_bf16_f32 v80, v80, s0
	ds_write_b16 v78, v80 offset:20016
	v_mul_f32_e32 v80, v2, v94
	v_cvt_pk_bf16_f32 v80, v80, s0
	ds_write_b16 v78, v80 offset:1728
	v_mul_f32_e32 v80, v1, v94
	v_mul_f32_e32 v76, 0x3db504f3, v76
	v_cvt_pk_bf16_f32 v80, v80, s0
	ds_write_b16 v78, v80 offset:20160
	v_mul_f32_e32 v80, v2, v76
	v_mul_f32_e32 v76, v1, v76
	v_mul_f32_e32 v95, 0x3db504f3, v100
	v_cvt_pk_bf16_f32 v76, v76, s0
	ds_write_b16 v78, v76 offset:20304
	v_mul_f32_e32 v76, v2, v95
	v_mul_f32_e32 v77, 0x3db504f3, v77
	v_cvt_pk_bf16_f32 v76, v76, s0
	ds_write_b16 v78, v76 offset:2016
	v_mul_f32_e32 v76, v1, v95
	v_mul_f32_e32 v2, v2, v77
	v_mul_f32_e32 v1, v1, v77
	v_cvt_pk_bf16_f32 v2, v2, s0
	v_cvt_pk_bf16_f32 v1, v1, s0
	v_cvt_pk_bf16_f32 v76, v76, s0
	ds_write_b16 v78, v2 offset:2160
	ds_write_b16 v78, v1 offset:20592
	v_lshlrev_b32_e32 v1, 1, v79
	v_lshlrev_b32_e32 v2, 1, v97
	v_readlane_b32 s7, v254, 45
	v_cvt_pk_bf16_f32 v96, v96, s0
	v_cvt_pk_bf16_f32 v83, v83, s0
	v_cvt_pk_bf16_f32 v80, v80, s0
	ds_write_b16 v78, v76 offset:20448
	v_add3_u32 v76, 0, v1, v2
	v_add3_u32 v1, 0, v2, v1
	v_cmp_gt_u32_e32 vcc, s92, v124
	v_mov_b32_e32 v2, s7
	s_sub_i32 s5, s5, s4
	ds_write_b16 v78, v96
	ds_write_b16 v78, v83 offset:1296
	ds_write_b16 v78, v80 offset:1872
	ds_write_b16 v76, v68 offset:36864
	ds_write_b16 v1, v72 offset:38016
	ds_write_b16_d16_hi v76, v68 offset:37008
	ds_write_b16_d16_hi v1, v72 offset:38160
	ds_write_b16 v76, v69 offset:37152
	ds_write_b16 v1, v73 offset:38304
	ds_write_b16_d16_hi v76, v69 offset:37296
	ds_write_b16_d16_hi v1, v73 offset:38448
	ds_write_b16 v76, v70 offset:37440
	ds_write_b16 v1, v74 offset:38592
	ds_write_b16_d16_hi v76, v70 offset:37584
	ds_write_b16_d16_hi v1, v74 offset:38736
	ds_write_b16 v76, v71 offset:37728
	ds_write_b16 v1, v75 offset:38880
	ds_write_b16_d16_hi v76, v71 offset:37872
	ds_write_b16_d16_hi v1, v75 offset:39024
	v_cndmask_b32_e64 v98, v2, 0, vcc
	v_mov_b32_e32 v2, s5
	v_mov_b32_e32 v68, s4
	v_ashrrev_i32_e32 v1, 8, v124
	v_cndmask_b32_e32 v68, v2, v68, vcc
	v_add_u32_e32 v1, s6, v1
	v_ashrrev_i32_e32 v69, 31, v68
	v_mad_i64_i32 v[68:69], s[4:5], v1, 36, v[68:69]
	v_readlane_b32 s4, v254, 6
	v_bfe_u32 v82, v124, 4, 2
	v_lshlrev_b64 v[68:69], 15, v[68:69]
	v_readlane_b32 s5, v254, 7
	v_lshlrev_b32_e32 v2, 3, v82
	v_and_b32_e32 v88, 15, v124
	v_lshl_add_u64 v[68:69], s[4:5], 0, v[68:69]
	v_lshl_add_u64 v[76:77], v[68:69], 0, v[2:3]
	v_lshrrev_b32_e32 v2, 1, v124
	v_and_b32_e32 v2, 0x60, v2
	v_or_b32_e32 v100, v2, v88
	v_mul_u32_u24_e32 v1, 0x90, v88
	v_lshlrev_b32_e32 v99, 4, v82
	v_mul_u32_u24_e32 v68, 0x90, v100
	v_add3_u32 v1, 0, v1, v99
	v_add3_u32 v72, v98, v68, v99
	v_lshlrev_b32_e32 v2, 1, v2
	s_waitcnt lgkmcnt(0)
	s_barrier
; DEVI unsigned cvt_pk(float lo, float hi) { f32x2 v = {lo, hi}; bf16x2_t b = __builtin_convertvector(v, bf16x2_t); return __builtin_bit_cast(unsigned, b); }
; DEVI void scan_a_ret(const Params& p, int l, int b, int h, int c, const RetIn& in, char* smem) {
;     ...
;     {   const int dir = wid >> 2;
;         const bf16_t* kT = dir ? kTb : kTf;
;         bf16_t* UT = (bf16_t*)(p.ws + WS_UTR) + ((size_t)((b * 4 + h) * 2 + dir) * NCH + order_idx(dir, c)) * (128 * 128);
; #pragma unroll
;         for (int q = 0; q < 2; ++q) { const int kkf = (wid & 3) * 2 + q;
;             const bf16x8 a0 = ldfrag(kT, 72, kkf * 16, 0, fr, fq), a1 = ldfrag(kT, 72, kkf * 16, 32, fr, fq);
; #pragma unroll
;             for (int vf = 0; vf < 8; ++vf) {
;                 f32x4 acc = {0.f, 0.f, 0.f, 0.f};
;                 acc = __builtin_amdgcn_mfma_f32_16x16x32_bf16(a0, ldfrag(vT, 72, vf * 16, 0, fr, fq), acc, 0, 0, 0);
;                 acc = __builtin_amdgcn_mfma_f32_16x16x32_bf16(a1, ldfrag(vT, 72, vf * 16, 32, fr, fq), acc, 0, 0, 0);
;                 *(u32x2*)(UT + (vf * 16 + fr) * 128 + kkf * 16 + fq * 4) = (u32x2){cvt_pk(acc[0], acc[1]), cvt_pk(acc[2], acc[3])};
;             } }
;     }
;     __syncthreads();
	ds_read_b128 v[68:71], v72
	ds_read_b128 v[72:75], v72 offset:64
	v_lshl_add_u64 v[96:97], v[76:77], 0, v[2:3]
	ds_read_b128 v[76:79], v1 offset:36864
	ds_read_b128 v[80:83], v1 offset:36928
	s_waitcnt lgkmcnt(1)
	v_mfma_f32_16x16x32_bf16 v[76:79], v[68:71], v[76:79], 0
	v_lshlrev_b32_e32 v2, 8, v88
	v_lshl_add_u64 v[90:91], v[96:97], 0, v[2:3]
	ds_read_b128 v[92:95], v1 offset:48448
	s_waitcnt lgkmcnt(1)
	v_mfma_f32_16x16x32_bf16 v[76:79], v[72:75], v[80:83], v[76:79]
	ds_read_b128 v[80:83], v1 offset:39232
	s_mov_b64 s[28:29], -1
	s_and_b64 vcc, s[44:45], exec
	s_nop 4
	v_cvt_pk_bf16_f32 v76, v76, v77
	v_cvt_pk_bf16_f32 v77, v78, v79
	global_store_dwordx2 v[90:91], v[76:77], off
	ds_read_b128 v[76:79], v1 offset:39168
	s_waitcnt lgkmcnt(0)
	v_mfma_f32_16x16x32_bf16 v[76:79], v[68:71], v[76:79], 0
	v_mfma_f32_16x16x32_bf16 v[76:79], v[72:75], v[80:83], v[76:79]
	ds_read_b128 v[80:83], v1 offset:41536
	s_nop 6
	v_cvt_pk_bf16_f32 v76, v76, v77
	v_cvt_pk_bf16_f32 v77, v78, v79
	v_or_b32_e32 v78, 0x1000, v2
	v_mov_b32_e32 v79, v3
	v_lshl_add_u64 v[88:89], v[96:97], 0, v[78:79]
	global_store_dwordx2 v[88:89], v[76:77], off
	ds_read_b128 v[76:79], v1 offset:41472
	s_waitcnt lgkmcnt(0)
	v_mfma_f32_16x16x32_bf16 v[76:79], v[68:71], v[76:79], 0
	v_mfma_f32_16x16x32_bf16 v[76:79], v[72:75], v[80:83], v[76:79]
	ds_read_b128 v[80:83], v1 offset:43840
	s_nop 6
	v_cvt_pk_bf16_f32 v76, v76, v77
	v_cvt_pk_bf16_f32 v77, v78, v79
	v_or_b32_e32 v78, 0x2000, v2
	v_mov_b32_e32 v79, v3
	v_lshl_add_u64 v[86:87], v[96:97], 0, v[78:79]
	global_store_dwordx2 v[86:87], v[76:77], off
	ds_read_b128 v[76:79], v1 offset:43776
	s_waitcnt lgkmcnt(0)
	v_mfma_f32_16x16x32_bf16 v[76:79], v[68:71], v[76:79], 0
	v_mfma_f32_16x16x32_bf16 v[76:79], v[72:75], v[80:83], v[76:79]
	ds_read_b128 v[80:83], v1 offset:46144
	s_nop 6
	v_cvt_pk_bf16_f32 v76, v76, v77
	v_cvt_pk_bf16_f32 v77, v78, v79
	v_or_b32_e32 v78, 0x3000, v2
	v_mov_b32_e32 v79, v3
	v_lshl_add_u64 v[84:85], v[96:97], 0, v[78:79]
	global_store_dwordx2 v[84:85], v[76:77], off
	ds_read_b128 v[76:79], v1 offset:46080
	s_waitcnt lgkmcnt(0)
	v_mfma_f32_16x16x32_bf16 v[76:79], v[68:71], v[76:79], 0
	v_mfma_f32_16x16x32_bf16 v[76:79], v[72:75], v[80:83], v[76:79]
	s_nop 7
	v_cvt_pk_bf16_f32 v76, v76, v77
	v_cvt_pk_bf16_f32 v77, v78, v79
	v_or_b32_e32 v78, 0x4000, v2
	v_mov_b32_e32 v79, v3
	v_lshl_add_u64 v[82:83], v[96:97], 0, v[78:79]
	global_store_dwordx2 v[82:83], v[76:77], off
	ds_read_b128 v[76:79], v1 offset:48384
	s_waitcnt lgkmcnt(0)
	v_mfma_f32_16x16x32_bf16 v[76:79], v[68:71], v[76:79], 0
	v_mfma_f32_16x16x32_bf16 v[76:79], v[72:75], v[92:95], v[76:79]
	ds_read_b128 v[92:95], v1 offset:50752
	s_nop 6
	v_cvt_pk_bf16_f32 v76, v76, v77
	v_cvt_pk_bf16_f32 v77, v78, v79
	v_or_b32_e32 v78, 0x5000, v2
	v_mov_b32_e32 v79, v3
	v_lshl_add_u64 v[80:81], v[96:97], 0, v[78:79]
	global_store_dwordx2 v[80:81], v[76:77], off
	ds_read_b128 v[76:79], v1 offset:50688
	s_waitcnt lgkmcnt(0)
	v_mfma_f32_16x16x32_bf16 v[76:79], v[68:71], v[76:79], 0
	v_mfma_f32_16x16x32_bf16 v[76:79], v[72:75], v[92:95], v[76:79]
	ds_read_b128 v[92:95], v1 offset:52992
	s_waitcnt lgkmcnt(0)
	v_mfma_f32_16x16x32_bf16 v[68:71], v[68:71], v[92:95], 0
	ds_read_b128 v[92:95], v1 offset:53056
	s_nop 3
	v_cvt_pk_bf16_f32 v76, v76, v77
	v_cvt_pk_bf16_f32 v77, v78, v79
	s_waitcnt lgkmcnt(0)
	v_mfma_f32_16x16x32_bf16 v[68:71], v[72:75], v[92:95], v[68:71]
	v_or_b32_e32 v78, 0x6000, v2
	v_mov_b32_e32 v79, v3
	v_lshl_add_u64 v[78:79], v[96:97], 0, v[78:79]
	v_or_b32_e32 v2, 0x7000, v2
	global_store_dwordx2 v[78:79], v[76:77], off
	v_lshl_add_u64 v[76:77], v[96:97], 0, v[2:3]
	v_or_b32_e32 v2, 16, v100
	s_nop 0
	v_cvt_pk_bf16_f32 v68, v68, v69
	v_cvt_pk_bf16_f32 v69, v70, v71
	v_mul_u32_u24_e32 v2, 0x90, v2
	global_store_dwordx2 v[76:77], v[68:69], off
	v_add3_u32 v2, v98, v2, v99
	ds_read_b128 v[72:75], v2
	ds_read_b128 v[68:71], v2 offset:64
	ds_read_b128 v[92:95], v1 offset:36864
	ds_read_b128 v[96:99], v1 offset:36928
	s_waitcnt lgkmcnt(1)
	v_mfma_f32_16x16x32_bf16 v[92:95], v[72:75], v[92:95], 0
	s_waitcnt lgkmcnt(0)
	v_mfma_f32_16x16x32_bf16 v[92:95], v[68:71], v[96:99], v[92:95]
	s_nop 7
	v_cvt_pk_bf16_f32 v92, v92, v93
	v_cvt_pk_bf16_f32 v93, v94, v95
	global_store_dwordx2 v[90:91], v[92:93], off offset:32
	ds_read_b128 v[90:93], v1 offset:39168
	ds_read_b128 v[94:97], v1 offset:39232
	s_waitcnt lgkmcnt(1)
	v_mfma_f32_16x16x32_bf16 v[90:93], v[72:75], v[90:93], 0
	s_waitcnt lgkmcnt(0)
	v_mfma_f32_16x16x32_bf16 v[90:93], v[68:71], v[94:97], v[90:93]
	s_nop 7
	v_cvt_pk_bf16_f32 v90, v90, v91
	v_cvt_pk_bf16_f32 v91, v92, v93
	global_store_dwordx2 v[88:89], v[90:91], off offset:32
	ds_read_b128 v[88:91], v1 offset:41472
	ds_read_b128 v[92:95], v1 offset:41536
	s_waitcnt lgkmcnt(1)
	v_mfma_f32_16x16x32_bf16 v[88:91], v[72:75], v[88:91], 0
	s_waitcnt lgkmcnt(0)
	v_mfma_f32_16x16x32_bf16 v[88:91], v[68:71], v[92:95], v[88:91]
	s_nop 7
	v_cvt_pk_bf16_f32 v88, v88, v89
	v_cvt_pk_bf16_f32 v89, v90, v91
	global_store_dwordx2 v[86:87], v[88:89], off offset:32
	ds_read_b128 v[86:89], v1 offset:43776
	ds_read_b128 v[90:93], v1 offset:43840
	s_waitcnt lgkmcnt(1)
	v_mfma_f32_16x16x32_bf16 v[86:89], v[72:75], v[86:89], 0
	s_waitcnt lgkmcnt(0)
	v_mfma_f32_16x16x32_bf16 v[86:89], v[68:71], v[90:93], v[86:89]
	s_nop 7
	v_cvt_pk_bf16_f32 v86, v86, v87
	v_cvt_pk_bf16_f32 v87, v88, v89
	global_store_dwordx2 v[84:85], v[86:87], off offset:32
	ds_read_b128 v[84:87], v1 offset:46080
	ds_read_b128 v[88:91], v1 offset:46144
	s_waitcnt lgkmcnt(1)
	v_mfma_f32_16x16x32_bf16 v[84:87], v[72:75], v[84:87], 0
	s_waitcnt lgkmcnt(0)
	v_mfma_f32_16x16x32_bf16 v[84:87], v[68:71], v[88:91], v[84:87]
	s_nop 7
	v_cvt_pk_bf16_f32 v84, v84, v85
	v_cvt_pk_bf16_f32 v85, v86, v87
	global_store_dwordx2 v[82:83], v[84:85], off offset:32
	ds_read_b128 v[82:85], v1 offset:48384
	ds_read_b128 v[86:89], v1 offset:48448
	s_waitcnt lgkmcnt(1)
	v_mfma_f32_16x16x32_bf16 v[82:85], v[72:75], v[82:85], 0
	s_waitcnt lgkmcnt(0)
	v_mfma_f32_16x16x32_bf16 v[82:85], v[68:71], v[86:89], v[82:85]
	s_nop 7
	v_cvt_pk_bf16_f32 v82, v82, v83
	v_cvt_pk_bf16_f32 v83, v84, v85
	global_store_dwordx2 v[80:81], v[82:83], off offset:32
	ds_read_b128 v[80:83], v1 offset:50688
	ds_read_b128 v[84:87], v1 offset:50752
	s_waitcnt lgkmcnt(1)
	v_mfma_f32_16x16x32_bf16 v[80:83], v[72:75], v[80:83], 0
	s_waitcnt lgkmcnt(0)
	v_mfma_f32_16x16x32_bf16 v[80:83], v[68:71], v[84:87], v[80:83]
	s_nop 7
	v_cvt_pk_bf16_f32 v80, v80, v81
	v_cvt_pk_bf16_f32 v81, v82, v83
	global_store_dwordx2 v[78:79], v[80:81], off offset:32
	ds_read_b128 v[78:81], v1 offset:52992
	s_waitcnt lgkmcnt(0)
	v_mfma_f32_16x16x32_bf16 v[72:75], v[72:75], v[78:81], 0
	ds_read_b128 v[78:81], v1 offset:53056
	s_waitcnt lgkmcnt(0)
	v_mfma_f32_16x16x32_bf16 v[68:71], v[68:71], v[78:81], v[72:75]
	s_nop 7
	v_cvt_pk_bf16_f32 v68, v68, v69
	v_cvt_pk_bf16_f32 v69, v70, v71
	global_store_dwordx2 v[76:77], v[68:69], off offset:32
	s_barrier
; #define SUB(n) if constexpr ((SUBMASK >> (n)) & 1)
; DEVI void cvt8_finish(const Params& p, int L, int t, const CvtIn& in, char* smem) {
;     const int which = t / 4096, r = t % 4096, le = L * 16 + r / 256, kt = (r % 256) / 16, nt = r % 16;
;     unsigned char* dst = (which == 2) ? (unsigned char*)(p.ws + WS_WDN) + (size_t)le * 2048 * 2048 + (size_t)(nt * 128) * 2048
;                                       : (unsigned char*)(p.ws + WS_WGU) + (size_t)le * 4096 * 2048 + (size_t)(nt * 256 + which * 128) * 2048;
; DEVI void phase_l2(const Params& p, int l, char* smem) {
;     ...
;             while (have) { const int un = u + G; const bool hn = un < nsc; RetIn nxt; const int r = u - nG, rn = un - nG;
;                 if (hn) ret_load(p, (rn / NCH) >> 2, (rn / NCH) & 3, rn % NCH, false, nxt);
;                 CvtIn ci; cvt8_load(p, l, (l == 0 ? TS0A : TS1A) + u, ci);
;                 SUB(3) scan_a_ret(p, l, (r / NCH) >> 2, (r / NCH) & 3, r % NCH, cur, smem);
;                 cvt8_finish(p, l, (l == 0 ? TS0A : TS1A) + u, ci, smem);
;                 cur = nxt; u = un; have = hn; } }
	s_cbranch_vccz .LBB0_533
	s_ashr_i32 s6, s24, 12
	s_lshl_b64 s[4:5], s[42:43], 23
	s_add_u32 s7, s37, s4
	s_addc_u32 s17, s78, s5
	s_lshl_b32 s4, s23, 8
	s_lshl_b32 s5, s6, 7
	s_add_i32 s4, s4, s5
	s_ashr_i32 s5, s4, 31
	s_lshl_b64 s[4:5], s[4:5], 11
	s_add_u32 s16, s7, s4
	s_addc_u32 s17, s17, s5
	s_mov_b64 s[28:29], 0

; DEVI int opaque_tid() { int t = threadIdx.x; asm volatile("" : "+v"(t)); return t; }
; DEVI int chunk_row0(int b, int c) { return (c < 4) ? (NLAT + b * CL + c * 64) : (b * SEQ + (c - 4) * 64); }
; DEVI void ret_decays(int h, float& ldf, float& ldb) { ldf = log1pf(-exp2f(-(5.f + 2.f * h))); ldb = log1pf(-exp2f(-(6.f + 2.f * h))); }
; DEVI void scan_c_ret(const Params& p, int l, int b, int h, int c, const RetIn& in, char* smem) {
;     float* obuf = (float*)smem;
;     bf16_t* qs = (bf16_t*)(smem + 32768); bf16_t* ks = qs + 64 * 136; bf16_t* vT = ks + 64 * 136; bf16_t* att = vT + 128 * 72;
;     const int tid = opaque_tid(), wid = tid >> 6, lane = tid & 63, fr = lane & 15, fq = lane >> 4;
;     const int row0 = chunk_row0(b, c); const bool lat = c >= 4;
;     const int tk = tid >> 3, kk16 = (tid & 7) * 16;
;     float ldf, ldb; ret_decays(h, ldf, ldb);
;     const bf16x8 gt0 = in.g0, gt1 = in.g1;
;     const bf16_t* SF = (const bf16_t*)(p.ws + WS_STR) + ((size_t)((b * 4 + h) * 2 + 0) * NCH + order_idx(0, c)) * 16384;
;     const bf16_t* SB = (const bf16_t*)(p.ws + WS_STR) + ((size_t)((b * 4 + h) * 2 + 1) * NCH + order_idx(1, c)) * 16384;
;     bf16x8 sff[4], sbf[4];
; #pragma unroll
;     for (int ksx = 0; ksx < 4; ++ksx) { sff[ksx] = *(const bf16x8*)(SF + (wid * 16 + fr) * 128 + ksx * 32 + fq * 8); sbf[ksx] = *(const bf16x8*)(SB + (wid * 16 + fr) * 128 + ksx * 32 + fq * 8); }
;     {   float qf[16], kf[16];
;         ret_rot(in.q0, in.q1, in, lat, 1.f, qf);
;         ret_rot(in.k0, in.k1, in, lat, 0.08838834764831845f, kf);
;         float t0[8], t1[8];
; #pragma unroll
;         for (int e = 0; e < 8; ++e) { t0[e] = qf[e]; t1[e] = qf[8 + e]; }
;         *(bf16x8*)(qs + tk * 136 + kk16) = pack8(t0); *(bf16x8*)(qs + tk * 136 + kk16 + 8) = pack8(t1);
; #pragma unroll
;         for (int e = 0; e < 8; ++e) { t0[e] = kf[e]; t1[e] = kf[8 + e]; }
;         *(bf16x8*)(ks + tk * 136 + kk16) = pack8(t0); *(bf16x8*)(ks + tk * 136 + kk16 + 8) = pack8(t1);
;         const bf16x8 v0 = in.v0, v1 = in.v1;
; #pragma unroll
;         for (int e = 0; e < 8; ++e) { vT[(kk16 + e) * 72 + tk] = (bf16_t)v0[e]; vT[(kk16 + 8 + e) * 72 + tk] = (bf16_t)v1[e]; }
;     }
;     __syncthreads();
.LBB0_768:
	v_mov_b32_e32 v214, 0xbc8102b3
	v_mov_b32_e32 v216, 0xbb80402b
	v_cmp_eq_u32_e64 vcc, s29, 1
	v_cndmask_b32_e32 v214, v214, v216, vcc
	v_mov_b32_e32 v216, 0xba801003
	v_cmp_eq_u32_e64 vcc, s29, 2
	v_cndmask_b32_e32 v214, v214, v216, vcc
	v_mov_b32_e32 v216, 0xb9800400
	v_cmp_eq_u32_e64 vcc, s29, 3
	v_cndmask_b32_e32 v214, v214, v216, vcc
	v_mov_b32_e32 v215, 0xbd020aec
	v_mov_b32_e32 v216, 0xbc0080ac
	v_cmp_eq_u32_e64 vcc, s29, 1
	v_cndmask_b32_e32 v215, v215, v216, vcc
	v_mov_b32_e32 v216, 0xbb00200b
	v_cmp_eq_u32_e64 vcc, s29, 2
	v_cndmask_b32_e32 v215, v215, v216, vcc
	v_mov_b32_e32 v216, 0xba000801
	v_cmp_eq_u32_e64 vcc, s29, 3
	v_cndmask_b32_e32 v215, v215, v216, vcc
	s_add_i32 s5, s4, 6
	v_cvt_f32_ubyte0_e32 v134, s5
	s_mov_b32 s33, 0x42fc0000
	v_cmp_lt_f32_e32 vcc, s33, v134
	s_and_b64 s[16:17], vcc, exec
	s_cselect_b32 s5, 0xffffffc0, 0
	v_cndmask_b32_e32 v135, 0, v226, vcc
	v_sub_f32_e32 v134, v135, v134
	v_exp_f32_e32 v134, v134
	s_mov_b32 s50, 0x3f317218
	s_add_i32 s4, s4, 5
	v_ldexp_f32 v180, v134, s5
	s_mov_b32 s16, 0x33800000
	v_cmp_gt_f32_e64 s[38:39], s16, v180
	v_lshlrev_b32_e32 v182, 3, v199
	v_cvt_f32_ubyte0_e32 v135, s4
	s_nop 0
	v_cmp_lt_f32_e32 vcc, s33, v135
	s_and_b64 s[4:5], vcc, exec
	s_cselect_b32 s4, 0xffffffc0, 0
	v_cndmask_b32_e32 v138, 0, v226, vcc
	v_sub_f32_e32 v135, v138, v135
	v_exp_f32_e32 v138, v135
	v_mov_b32_e32 v135, v214
	v_readlane_b32 s33, v254, 48
	s_lshl_b32 s52, s29, 8
	v_ldexp_f32 v183, v138, s4
	s_mov_b32 s4, 0x3db504f3
	s_movk_i32 s17, 0x110
	v_pk_mov_b32 v[144:145], v[178:179], v[140:141] op_sel:[1,0]
	v_mov_b32_e32 v179, v141
	v_lshlrev_b32_e32 v134, 4, v200
	v_pk_mov_b32 v[140:141], v[176:177], v[142:143] op_sel:[1,0]
	v_and_b32_e32 v138, 0x70, v134
	v_ashrrev_i32_e32 v134, 3, v200
	v_pk_mul_f32 v[148:149], v[140:141], s[4:5] op_sel_hi:[1,0]
	v_pk_mov_b32 v[140:141], v[174:175], v[136:137] op_sel:[1,0]
	v_mov_b32_e32 v177, v143
	v_pk_mul_f32 v[152:153], v[140:141], s[4:5] op_sel_hi:[1,0]
	v_pk_mov_b32 v[140:141], v[172:173], v[132:133] op_sel:[1,0]
	v_mov_b32_e32 v173, v133
	v_mul_lo_u32 v133, v134, s17
	v_lshlrev_b32_e32 v132, 1, v138
	v_pk_mul_f32 v[154:155], v[140:141], s[4:5] op_sel_hi:[1,0]
	v_cvt_pk_bf16_f32 v140, v164, v165
	v_cvt_pk_bf16_f32 v141, v166, v167
	v_cvt_pk_bf16_f32 v142, v168, v169
	v_cvt_pk_bf16_f32 v143, v170, v171
	v_add3_u32 v133, 0, v133, v132
	v_pk_mul_f32 v[144:145], v[144:145], s[4:5] op_sel_hi:[1,0]
	v_pk_mul_f32 v[146:147], v[178:179], s[4:5] op_sel_hi:[1,0]
	v_pk_mul_f32 v[150:151], v[176:177], s[4:5] op_sel_hi:[1,0]
	v_mov_b32_e32 v175, v137
	ds_write_b128 v133, v[140:143] offset:32768
	v_cvt_pk_bf16_f32 v140, v160, v161
	v_cvt_pk_bf16_f32 v141, v156, v157
	v_cvt_pk_bf16_f32 v142, v162, v163
	v_cvt_pk_bf16_f32 v143, v158, v159
	v_pk_mul_f32 v[136:137], v[174:175], s[4:5] op_sel_hi:[1,0]
	v_pk_mul_f32 v[172:173], v[172:173], s[4:5] op_sel_hi:[1,0]
	ds_write_b128 v133, v[140:143] offset:32784
	v_cvt_pk_bf16_f32 v140, v144, v145
	v_cvt_pk_bf16_f32 v141, v146, v147
	v_cvt_pk_bf16_f32 v142, v148, v149
	v_cvt_pk_bf16_f32 v143, v150, v151
	ds_write_b128 v133, v[140:143] offset:50176
	v_cvt_pk_bf16_f32 v140, v152, v153
	v_cvt_pk_bf16_f32 v141, v136, v137
	v_cvt_pk_bf16_f32 v142, v154, v155
	v_cvt_pk_bf16_f32 v143, v172, v173
	v_mul_u32_u24_e32 v136, 0x48, v138
	ds_write_b128 v133, v[140:143] offset:50192
	v_lshlrev_b32_e32 v133, 1, v134
	v_lshlrev_b32_e32 v136, 1, v136
	v_add3_u32 v137, s33, v133, v136
	v_add3_u32 v133, s33, v136, v133
	ds_write_b16 v137, v92
	ds_write_b16 v133, v96 offset:1152
	ds_write_b16_d16_hi v137, v92 offset:144
	ds_write_b16_d16_hi v137, v96 offset:1296
	ds_write_b16 v137, v93 offset:288
	ds_write_b16 v133, v97 offset:1440
	ds_write_b16_d16_hi v137, v93 offset:432
	ds_write_b16_d16_hi v133, v97 offset:1584
	ds_write_b16 v137, v94 offset:576
	ds_write_b16 v133, v98 offset:1728
	ds_write_b16_d16_hi v137, v94 offset:720
	ds_write_b16_d16_hi v133, v98 offset:1872
	ds_write_b16 v137, v95 offset:864
	ds_write_b16 v133, v99 offset:2016
	ds_write_b16_d16_hi v137, v95 offset:1008
	ds_write_b16_d16_hi v133, v99 offset:2160
	v_lshlrev_b32_e32 v133, 4, v198
	v_and_b32_e32 v137, 48, v133
	v_lshlrev_b32_e32 v156, 1, v182
	v_or_b32_e32 v92, v137, v1
	v_add_u32_e32 v136, 0, v156
	v_mad_u32_u24 v154, v92, s17, v136
	s_waitcnt lgkmcnt(0)
	s_barrier
; DEVI unsigned cvt_pk(float lo, float hi) { f32x2 v = {lo, hi}; bf16x2_t b = __builtin_convertvector(v, bf16x2_t); return __builtin_bit_cast(unsigned, b); }
; DEVI void scan_c_ret(const Params& p, int l, int b, int h, int c, const RetIn& in, char* smem) {
;     ...
;     {   const int jf = wid & 3;
; #pragma unroll
;         for (int q = 0; q < 2; ++q) { const int iff = (wid >> 2) * 2 + q;
;             f32x4 a = {0.f, 0.f, 0.f, 0.f};
; #pragma unroll
;             for (int ksx = 0; ksx < 4; ++ksx) a = __builtin_amdgcn_mfma_f32_16x16x32_bf16(ldfrag(ks, 136, jf * 16, ksx * 32, fr, fq), ldfrag(qs, 136, iff * 16, ksx * 32, fr, fq), a, 0, 0, 0);
;             const int i = iff * 16 + fr, j0 = jf * 16 + fq * 4;
;             float r[4];
; #pragma unroll
;             for (int e = 0; e < 4; ++e) { const int j = j0 + e; r[e] = a[e] * ((j <= i) ? __expf(ldf * (float)(i - j)) : __expf(ldb * (float)(j - i))); }
;             *(u32x2*)(att + i * 72 + j0) = (u32x2){cvt_pk(r[0], r[1]), cvt_pk(r[2], r[3])};
;         }
;     }
;     __syncthreads();
	ds_read_b128 v[92:95], v154 offset:50176
	s_movk_i32 s4, 0xffe0
	v_and_or_b32 v155, v134, s4, v1
	v_mad_u64_u32 v[152:153], s[4:5], v155, s17, v[136:137]
	ds_read_b128 v[96:99], v152 offset:32768
	ds_read_b128 v[140:143], v154 offset:50240
	ds_read_b128 v[144:147], v152 offset:32832
	s_waitcnt lgkmcnt(2)
	v_mfma_f32_16x16x32_bf16 v[92:95], v[92:95], v[96:99], 0
	ds_read_b128 v[96:99], v154 offset:50304
	v_lshl_or_b32 v137, v199, 2, v137
	v_sub_u32_e32 v157, v137, v155
	v_sub_u32_e32 v158, 0, v157
	s_waitcnt lgkmcnt(1)
	v_mfma_f32_16x16x32_bf16 v[92:95], v[140:143], v[144:147], v[92:95]
	ds_read_b128 v[140:143], v154 offset:50368
	ds_read_b128 v[144:147], v152 offset:32896
	ds_read_b128 v[148:151], v152 offset:32960
	v_max_i32_e32 v157, v157, v158
	v_cvt_f32_u32_e32 v157, v157
	v_cmp_gt_f32_e32 vcc, s16, v183
	s_waitcnt lgkmcnt(1)
	v_mfma_f32_16x16x32_bf16 v[92:95], v[96:99], v[144:147], v[92:95]
	v_or_b32_e32 v158, 2, v137
	v_mov_b32_e32 v139, v215
	v_cmp_gt_i32_e32 vcc, v137, v155
	v_or_b32_e32 v159, 3, v137
	s_waitcnt lgkmcnt(0)
	v_mfma_f32_16x16x32_bf16 v[92:95], v[140:143], v[148:151], v[92:95]
	v_cndmask_b32_e32 v96, v139, v135, vcc
	v_mul_f32_e32 v96, v96, v157
	v_or_b32_e32 v157, 1, v137
	v_sub_u32_e32 v97, v157, v155
	v_sub_u32_e32 v98, v155, v157
	v_cmp_lt_i32_e32 vcc, v137, v155
	v_mul_f32_e32 v96, 0x3fb8aa3b, v96
	v_exp_f32_e32 v96, v96
	v_cndmask_b32_e32 v97, v97, v98, vcc
	v_cvt_f32_i32_e32 v97, v97
	v_cndmask_b32_e32 v98, v135, v139, vcc
	v_cmp_gt_i32_e32 vcc, v158, v155
	s_add_i32 s4, 0, 0x15000
	v_mul_f32_e32 v97, v98, v97
	v_sub_u32_e32 v98, v158, v155
	v_sub_u32_e32 v99, 0, v98
	v_max_i32_e32 v98, v98, v99
	v_cvt_f32_u32_e32 v98, v98
	v_cndmask_b32_e32 v99, v139, v135, vcc
	v_cmp_gt_i32_e32 vcc, v159, v155
	v_mul_f32_e32 v97, 0x3fb8aa3b, v97
	v_mul_f32_e32 v98, v99, v98
	v_sub_u32_e32 v99, v159, v155
	v_sub_u32_e32 v144, 0, v99
	v_max_i32_e32 v99, v99, v144
	v_cvt_f32_u32_e32 v99, v99
	v_cndmask_b32_e32 v144, v139, v135, vcc
	v_mul_f32_e32 v98, 0x3fb8aa3b, v98
	v_exp_f32_e32 v97, v97
	v_mul_f32_e32 v99, v144, v99
	v_mul_f32_e32 v99, 0x3fb8aa3b, v99
	v_exp_f32_e32 v98, v98
	v_exp_f32_e32 v99, v99
	v_pk_mul_f32 v[92:93], v[96:97], v[92:93]
	v_lshlrev_b32_e32 v153, 1, v137
	v_cvt_pk_bf16_f32 v92, v92, v93
	v_pk_mul_f32 v[94:95], v[98:99], v[94:95]
	v_or_b32_e32 v133, v133, v1
	v_cvt_pk_bf16_f32 v93, v94, v95
	v_mul_lo_u32 v94, v155, s91
	v_add3_u32 v153, s4, v153, v94
	ds_write_b64 v153, v[92:93]
	ds_read_b128 v[92:95], v154 offset:50176
	ds_read_b128 v[96:99], v154 offset:50240
	ds_read_b128 v[140:143], v152 offset:37120
	ds_read_b128 v[144:147], v152 offset:37184
	s_waitcnt lgkmcnt(1)
	v_mfma_f32_16x16x32_bf16 v[92:95], v[92:95], v[140:143], 0
	ds_read_b128 v[140:143], v154 offset:50304
	v_or_b32_e32 v155, 16, v155
	v_cmp_gt_i32_e32 vcc, v137, v155
	s_waitcnt lgkmcnt(1)
	v_mfma_f32_16x16x32_bf16 v[92:95], v[96:99], v[144:147], v[92:95]
	ds_read_b128 v[96:99], v154 offset:50368
	ds_read_b128 v[144:147], v152 offset:37248
	ds_read_b128 v[148:151], v152 offset:37312
	v_sub_u32_e32 v152, v137, v155
	v_sub_u32_e32 v154, 0, v152
	s_waitcnt lgkmcnt(1)
	v_mfma_f32_16x16x32_bf16 v[92:95], v[140:143], v[144:147], v[92:95]
	v_cndmask_b32_e32 v140, v139, v135, vcc
	v_sub_u32_e32 v141, v157, v155
	v_sub_u32_e32 v142, v155, v157
	v_cmp_lt_i32_e32 vcc, v137, v155
	v_max_i32_e32 v152, v152, v154
	v_cvt_f32_u32_e32 v152, v152
	v_cndmask_b32_e32 v137, v141, v142, vcc
	v_cvt_f32_i32_e32 v137, v137
	v_cndmask_b32_e32 v141, v135, v139, vcc
	v_cmp_gt_i32_e32 vcc, v158, v155
	v_mul_f32_e32 v140, v140, v152
	v_mul_f32_e32 v137, v141, v137
	v_sub_u32_e32 v141, v158, v155
	v_sub_u32_e32 v142, 0, v141
	v_max_i32_e32 v141, v141, v142
	v_cvt_f32_u32_e32 v142, v141
	v_mul_f32_e32 v137, 0x3fb8aa3b, v137
	v_exp_f32_e32 v141, v137
	v_cndmask_b32_e32 v137, v139, v135, vcc
	v_mul_f32_e32 v137, v137, v142
	v_sub_u32_e32 v142, v159, v155
	v_sub_u32_e32 v143, 0, v142
	v_max_i32_e32 v142, v142, v143
	v_cvt_f32_u32_e32 v143, v142
	v_mul_f32_e32 v137, 0x3fb8aa3b, v137
	v_cmp_gt_i32_e32 vcc, v159, v155
	v_exp_f32_e32 v142, v137
	v_mul_f32_e32 v140, 0x3fb8aa3b, v140
	v_cndmask_b32_e32 v137, v139, v135, vcc
	v_mul_f32_e32 v137, v137, v143
	v_mul_f32_e32 v137, 0x3fb8aa3b, v137
	v_exp_f32_e32 v140, v140
	v_exp_f32_e32 v143, v137
	s_waitcnt lgkmcnt(0)
	v_mfma_f32_16x16x32_bf16 v[92:95], v[96:99], v[148:151], v[92:95]
	v_mad_u32_u24 v137, v1, s17, v136
	v_mul_lo_u32 v133, v133, s91
	v_add3_u32 v133, s33, v133, v156
	v_sub_u32_e32 v136, 64, v1
	v_cvt_f32_ubyte0_e32 v136, v136
	s_nop 2
	v_pk_mul_f32 v[92:93], v[140:141], v[92:93]
	v_pk_mul_f32 v[94:95], v[142:143], v[94:95]
	v_cvt_pk_bf16_f32 v92, v92, v93
	v_cvt_pk_bf16_f32 v93, v94, v95
	ds_write_b64 v153, v[92:93] offset:2304
	s_waitcnt lgkmcnt(0)
	s_barrier
; DEVI void scan_c_ret(const Params& p, int l, int b, int h, int c, const RetIn& in, char* smem) {
;     ...
;     {   const int vf = wid;
;         const bf16x8 vt0 = ldfrag(vT, 72, vf * 16, 0, fr, fq), vt1 = ldfrag(vT, 72, vf * 16, 32, fr, fq);
; #pragma unroll
;         for (int iff = 0; iff < 4; ++iff) {
;             const int i = iff * 16 + fr;
;             const float sf = __expf(ldf * (float)(i + 1)), sb = __expf(ldb * (float)(64 - i));
;             f32x4 acc = {0.f, 0.f, 0.f, 0.f}, accf = {0.f, 0.f, 0.f, 0.f}, accb = {0.f, 0.f, 0.f, 0.f};
;             acc = __builtin_amdgcn_mfma_f32_16x16x32_bf16(vt0, ldfrag(att, 72, iff * 16, 0, fr, fq), acc, 0, 0, 0);
;             acc = __builtin_amdgcn_mfma_f32_16x16x32_bf16(vt1, ldfrag(att, 72, iff * 16, 32, fr, fq), acc, 0, 0, 0);
; #pragma unroll
;             for (int ksx = 0; ksx < 4; ++ksx) { const bf16x8 qv = ldfrag(qs, 136, iff * 16, ksx * 32, fr, fq);
;                 accf = __builtin_amdgcn_mfma_f32_16x16x32_bf16(sff[ksx], qv, accf, 0, 0, 0);
;                 accb = __builtin_amdgcn_mfma_f32_16x16x32_bf16(sbf[ksx], qv, accb, 0, 0, 0); }
;             *(f32x4*)(obuf + i * 128 + vf * 16 + fq * 4) = acc + sf * accf + sb * accb;
;         }
;     }
	ds_read_b128 v[92:95], v137 offset:32768
	ds_read_b128 v[96:99], v137 offset:32832
	s_waitcnt vmcnt(7) lgkmcnt(1)
	v_mfma_f32_16x16x32_bf16 v[140:143], v[120:123], v[92:95], 0
	v_mul_f32_e32 v136, v135, v136
	v_mul_f32_e32 v136, 0x3fb8aa3b, v136
	v_exp_f32_e32 v136, v136
	s_waitcnt vmcnt(5)
	v_mfma_f32_16x16x32_bf16 v[92:95], v[128:131], v[92:95], 0
	v_or_b32_e32 v157, 16, v1
	s_waitcnt lgkmcnt(0)
	v_mfma_f32_16x16x32_bf16 v[140:143], v[116:119], v[96:99], v[140:143]
	s_waitcnt vmcnt(4)
	v_mfma_f32_16x16x32_bf16 v[92:95], v[124:127], v[96:99], v[92:95]
	ds_read_b128 v[96:99], v137 offset:32896
	ds_read_b128 v[144:147], v133
	ds_read_b128 v[148:151], v133 offset:64
	ds_read_b128 v[152:155], v137 offset:32960
	v_lshlrev_b32_e32 v133, 6, v198
	s_waitcnt vmcnt(3) lgkmcnt(3)
	v_mfma_f32_16x16x32_bf16 v[140:143], v[108:111], v[96:99], v[140:143]
	v_add3_u32 v133, 0, v133, v2
	v_add_u32_e32 v2, 1, v1
	v_cvt_f32_ubyte0_e32 v2, v2
	s_waitcnt vmcnt(1)
	v_mfma_f32_16x16x32_bf16 v[92:95], v[112:115], v[96:99], v[92:95]
	v_mul_f32_e32 v2, v139, v2
	v_mul_f32_e32 v2, 0x3fb8aa3b, v2
	v_exp_f32_e32 v2, v2
	s_waitcnt lgkmcnt(0)
	v_mfma_f32_16x16x32_bf16 v[96:99], v[104:107], v[152:155], v[140:143]
	s_nop 2
	v_mul_u32_u24_e32 v140, 0x90, v1
	v_add3_u32 v156, s4, v140, v156
	ds_read_b128 v[140:143], v156
	s_waitcnt vmcnt(0)
	v_mfma_f32_16x16x32_bf16 v[92:95], v[100:103], v[152:155], v[92:95]
	ds_read_b128 v[152:155], v156 offset:64
	s_mov_b64 s[4:5], 0x43caec00
	s_waitcnt lgkmcnt(1)
	v_mfma_f32_16x16x32_bf16 v[140:143], v[144:147], v[140:143], 0
	s_waitcnt lgkmcnt(0)
	v_mfma_f32_16x16x32_bf16 v[140:143], v[148:151], v[152:155], v[140:143]
	s_nop 7
	v_pk_fma_f32 v[98:99], v[2:3], v[98:99], v[142:143] op_sel_hi:[0,1,1]
	v_pk_fma_f32 v[96:97], v[2:3], v[96:97], v[140:141] op_sel_hi:[0,1,1]
	v_pk_fma_f32 v[92:93], v[136:137], v[92:93], v[96:97] op_sel_hi:[0,1,1]
	v_pk_fma_f32 v[94:95], v[136:137], v[94:95], v[98:99] op_sel_hi:[0,1,1]
	v_lshl_add_u32 v2, v1, 9, v133
	ds_write_b128 v2, v[92:95]
	ds_read_b128 v[92:95], v137 offset:37120
	ds_read_b128 v[96:99], v137 offset:37184
	s_waitcnt lgkmcnt(1)
	v_mfma_f32_16x16x32_bf16 v[140:143], v[120:123], v[92:95], 0
	v_add_u32_e32 v2, 17, v1
	v_cvt_f32_ubyte0_e32 v2, v2
	v_sub_u32_e32 v136, 64, v157
	v_mfma_f32_16x16x32_bf16 v[92:95], v[128:131], v[92:95], 0
	v_mul_f32_e32 v2, v139, v2
	v_cvt_f32_ubyte0_e32 v136, v136
	v_mul_f32_e32 v2, 0x3fb8aa3b, v2
	s_waitcnt lgkmcnt(0)
	v_mfma_f32_16x16x32_bf16 v[140:143], v[116:119], v[96:99], v[140:143]
	v_mul_f32_e32 v136, v135, v136
	v_mul_f32_e32 v136, 0x3fb8aa3b, v136
	v_exp_f32_e32 v2, v2
	v_mfma_f32_16x16x32_bf16 v[92:95], v[124:127], v[96:99], v[92:95]
	ds_read_b128 v[96:99], v137 offset:37248
	ds_read_b128 v[152:155], v137 offset:37312
	v_exp_f32_e32 v136, v136
	s_waitcnt lgkmcnt(1)
	v_mfma_f32_16x16x32_bf16 v[140:143], v[108:111], v[96:99], v[140:143]
	v_mfma_f32_16x16x32_bf16 v[92:95], v[112:115], v[96:99], v[92:95]
	s_waitcnt lgkmcnt(0)
	v_mfma_f32_16x16x32_bf16 v[96:99], v[104:107], v[152:155], v[140:143]
	s_nop 4
	ds_read_b128 v[140:143], v156 offset:2304
	v_mfma_f32_16x16x32_bf16 v[92:95], v[100:103], v[152:155], v[92:95]
	ds_read_b128 v[152:155], v156 offset:2368
	s_waitcnt lgkmcnt(1)
	v_mfma_f32_16x16x32_bf16 v[140:143], v[144:147], v[140:143], 0
	s_waitcnt lgkmcnt(0)
	v_mfma_f32_16x16x32_bf16 v[140:143], v[148:151], v[152:155], v[140:143]
	s_nop 7
	v_pk_fma_f32 v[98:99], v[2:3], v[98:99], v[142:143] op_sel_hi:[0,1,1]
	v_pk_fma_f32 v[96:97], v[2:3], v[96:97], v[140:141] op_sel_hi:[0,1,1]
	v_pk_fma_f32 v[92:93], v[136:137], v[92:93], v[96:97] op_sel_hi:[0,1,1]
	v_pk_fma_f32 v[94:95], v[136:137], v[94:95], v[98:99] op_sel_hi:[0,1,1]
	v_lshl_add_u32 v2, v157, 9, v133
	ds_write_b128 v2, v[92:95]
	ds_read_b128 v[92:95], v137 offset:41472
	ds_read_b128 v[96:99], v137 offset:41536
	s_waitcnt lgkmcnt(1)
	v_mfma_f32_16x16x32_bf16 v[140:143], v[120:123], v[92:95], 0
	v_or_b32_e32 v157, 32, v1
	v_add_u32_e32 v2, 33, v1
	v_cvt_f32_ubyte0_e32 v2, v2
	v_mfma_f32_16x16x32_bf16 v[92:95], v[128:131], v[92:95], 0
	v_sub_u32_e32 v136, 64, v157
	v_mul_f32_e32 v2, v139, v2
	v_cvt_f32_ubyte0_e32 v136, v136
	s_waitcnt lgkmcnt(0)
	v_mfma_f32_16x16x32_bf16 v[140:143], v[116:119], v[96:99], v[140:143]
	v_mul_f32_e32 v2, 0x3fb8aa3b, v2
	v_mul_f32_e32 v136, v135, v136
	v_mul_f32_e32 v136, 0x3fb8aa3b, v136
	v_mfma_f32_16x16x32_bf16 v[92:95], v[124:127], v[96:99], v[92:95]
	ds_read_b128 v[96:99], v137 offset:41600
	ds_read_b128 v[152:155], v137 offset:41664
	v_exp_f32_e32 v2, v2
	v_exp_f32_e32 v136, v136
	s_waitcnt lgkmcnt(1)
	v_mfma_f32_16x16x32_bf16 v[140:143], v[108:111], v[96:99], v[140:143]
	v_mfma_f32_16x16x32_bf16 v[92:95], v[112:115], v[96:99], v[92:95]
	s_waitcnt lgkmcnt(0)
	v_mfma_f32_16x16x32_bf16 v[96:99], v[104:107], v[152:155], v[140:143]
	s_nop 4
	ds_read_b128 v[140:143], v156 offset:4608
	v_mfma_f32_16x16x32_bf16 v[92:95], v[100:103], v[152:155], v[92:95]
	ds_read_b128 v[152:155], v156 offset:4672
	s_waitcnt lgkmcnt(1)
	v_mfma_f32_16x16x32_bf16 v[140:143], v[144:147], v[140:143], 0
	s_waitcnt lgkmcnt(0)
	v_mfma_f32_16x16x32_bf16 v[140:143], v[148:151], v[152:155], v[140:143]
	s_nop 7
	v_pk_fma_f32 v[98:99], v[2:3], v[98:99], v[142:143] op_sel_hi:[0,1,1]
	v_pk_fma_f32 v[96:97], v[2:3], v[96:97], v[140:141] op_sel_hi:[0,1,1]
	v_pk_fma_f32 v[92:93], v[136:137], v[92:93], v[96:97] op_sel_hi:[0,1,1]
	v_pk_fma_f32 v[94:95], v[136:137], v[94:95], v[98:99] op_sel_hi:[0,1,1]
	v_lshl_add_u32 v2, v157, 9, v133
	ds_write_b128 v2, v[92:95]
	ds_read_b128 v[92:95], v137 offset:45824
	ds_read_b128 v[96:99], v137 offset:45888
	s_waitcnt lgkmcnt(1)
; DEVI float silu_f(float x) { return x * __builtin_amdgcn_rcpf(1.f + __expf(-x)); }
; DEVI void scan_c_tail(const float* o, int tid, const bf16x8 g0, const bf16x8 g1, int row0, bf16_t* ymix, int ycol) {
;     ...
;     float ga[8], gb[8]; unpack8(g0, ga); unpack8(g1, gb);
;     float y0[8], y1[8];
; #pragma unroll
;     for (int i = 0; i < 8; ++i) { y0[i] = ov[i] * rstd * silu_f(ga[i]); y1[i] = ov[8 + i] * rstd * silu_f(gb[i]); }
; DEVI void scan_c_ret(const Params& p, int l, int b, int h, int c, const RetIn& in, char* smem) {
;     ...
;         for (int iff = 0; iff < 4; ++iff) {
;             const int i = iff * 16 + fr;
;             const float sf = __expf(ldf * (float)(i + 1)), sb = __expf(ldb * (float)(64 - i));
;             f32x4 acc = {0.f, 0.f, 0.f, 0.f}, accf = {0.f, 0.f, 0.f, 0.f}, accb = {0.f, 0.f, 0.f, 0.f};
;             acc = __builtin_amdgcn_mfma_f32_16x16x32_bf16(vt0, ldfrag(att, 72, iff * 16, 0, fr, fq), acc, 0, 0, 0);
;             acc = __builtin_amdgcn_mfma_f32_16x16x32_bf16(vt1, ldfrag(att, 72, iff * 16, 32, fr, fq), acc, 0, 0, 0);
; #pragma unroll
;             for (int ksx = 0; ksx < 4; ++ksx) { const bf16x8 qv = ldfrag(qs, 136, iff * 16, ksx * 32, fr, fq);
;                 accf = __builtin_amdgcn_mfma_f32_16x16x32_bf16(sff[ksx], qv, accf, 0, 0, 0);
;                 accb = __builtin_amdgcn_mfma_f32_16x16x32_bf16(sbf[ksx], qv, accb, 0, 0, 0); }
;             *(f32x4*)(obuf + i * 128 + vf * 16 + fq * 4) = acc + sf * accf + sb * accb;
;         }
	v_mfma_f32_16x16x32_bf16 v[120:123], v[120:123], v[92:95], 0
	v_mfma_f32_16x16x32_bf16 v[92:95], v[128:131], v[92:95], 0
	s_waitcnt lgkmcnt(0)
	v_mfma_f32_16x16x32_bf16 v[116:119], v[116:119], v[96:99], v[120:123]
	v_mfma_f32_16x16x32_bf16 v[92:95], v[124:127], v[96:99], v[92:95]
	ds_read_b128 v[96:99], v137 offset:45952
	s_nop 2
	ds_read_b128 v[120:123], v137 offset:46016
	s_waitcnt lgkmcnt(1)
	v_mfma_f32_16x16x32_bf16 v[108:111], v[108:111], v[96:99], v[116:119]
	s_nop 2
	v_or_b32_e32 v116, 48, v1
	v_mfma_f32_16x16x32_bf16 v[92:95], v[112:115], v[96:99], v[92:95]
	v_add_u32_e32 v1, 49, v1
	v_cvt_f32_ubyte0_e32 v1, v1
	v_sub_u32_e32 v2, 64, v116
	s_waitcnt lgkmcnt(0)
	v_mfma_f32_16x16x32_bf16 v[96:99], v[104:107], v[120:123], v[108:111]
	ds_read_b128 v[104:107], v156 offset:6912
	v_mul_f32_e32 v1, v139, v1
	v_cvt_f32_ubyte0_e32 v2, v2
	v_mfma_f32_16x16x32_bf16 v[92:95], v[100:103], v[120:123], v[92:95]
	ds_read_b128 v[100:103], v156 offset:6976
	v_mul_f32_e32 v1, 0x3fb8aa3b, v1
	v_mul_f32_e32 v2, v135, v2
	s_waitcnt lgkmcnt(1)
	v_mfma_f32_16x16x32_bf16 v[104:107], v[144:147], v[104:107], 0
	v_mul_f32_e32 v108, 0x3fb8aa3b, v2
	v_exp_f32_e32 v2, v1
	v_exp_f32_e32 v108, v108
	s_waitcnt lgkmcnt(0)
	v_mfma_f32_16x16x32_bf16 v[100:103], v[148:151], v[100:103], v[104:107]
	v_lshl_add_u32 v1, v116, 9, v133
	v_lshlrev_b32_e32 v112, 16, v52
	v_and_b32_e32 v113, 0xffff0000, v52
	v_mul_f32_e32 v52, 0xbfb8aa3b, v112
	v_exp_f32_e32 v52, v52
	s_nop 2
	v_pk_fma_f32 v[98:99], v[2:3], v[98:99], v[102:103] op_sel_hi:[0,1,1]
	v_pk_fma_f32 v[96:97], v[2:3], v[96:97], v[100:101] op_sel_hi:[0,1,1]
	v_pk_fma_f32 v[92:93], v[108:109], v[92:93], v[96:97] op_sel_hi:[0,1,1]
	v_pk_fma_f32 v[94:95], v[108:109], v[94:95], v[98:99] op_sel_hi:[0,1,1]
	ds_write_b128 v1, v[92:95]
	v_lshlrev_b32_e32 v1, 9, v134
	v_lshlrev_b32_e32 v2, 2, v138
	v_add3_u32 v1, 0, v1, v2
	s_waitcnt lgkmcnt(0)
	s_barrier
; #define SUB(n) if constexpr ((SUBMASK >> (n)) & 1)
; DEVI float silu_f(float x) { return x * __builtin_amdgcn_rcpf(1.f + __expf(-x)); }
; DEVI void scan_c_tail(const float* o, int tid, const bf16x8 g0, const bf16x8 g1, int row0, bf16_t* ymix, int ycol) {
;     const int tk = tid >> 3, v16 = (tid & 7) * 16;
;     float ov[16]; float ss = 0.f;
; #pragma unroll
;     for (int q = 0; q < 4; ++q) { const f32x4 t = *(const f32x4*)(o + tk * 128 + v16 + q * 4); ov[q * 4] = t[0]; ov[q * 4 + 1] = t[1]; ov[q * 4 + 2] = t[2]; ov[q * 4 + 3] = t[3]; }
; #pragma unroll
;     for (int i = 0; i < 16; ++i) ss += ov[i] * ov[i];
;     ss += __shfl_xor(ss, 1); ss += __shfl_xor(ss, 2); ss += __shfl_xor(ss, 4);
;     const float rstd = rsqrtf(ss * (1.f / 128.f) + EPS);
;     float ga[8], gb[8]; unpack8(g0, ga); unpack8(g1, gb);
;     float y0[8], y1[8];
; #pragma unroll
;     for (int i = 0; i < 8; ++i) { y0[i] = ov[i] * rstd * silu_f(ga[i]); y1[i] = ov[8 + i] * rstd * silu_f(gb[i]); }
;     *(bf16x8*)(ymix + (size_t)(row0 + tk) * DM + ycol + v16) = pack8(y0);
;     *(bf16x8*)(ymix + (size_t)(row0 + tk) * DM + ycol + v16 + 8) = pack8(y1);
; }
; DEVI void phase_l4(const Params& p, int l, char* smem) {
;     ...
;             while (have) { const int un = u + G; const bool hn = un < nsc; RetIn nxt; const int r = u - nG, rn = un - nG;
;                 if (hn) ret_load(p, (rn / ncs) >> 2, (rn / ncs) & 3, rn % ncs + c0, true, nxt);
;                 CvtIn ci; cvt8_load(p, l, (l == 0 ? TS0C : TS1C) + u, ci);
;                 SUB(6) scan_c_ret(p, l, (r / ncs) >> 2, (r / ncs) & 3, r % ncs + c0, cur, smem);
;                 cvt8_finish(p, l, (l == 0 ? TS0C : TS1C) + u, ci, smem);
;                 cur = nxt; u = un; have = hn; } }
	ds_read_b128 v[92:95], v1
	ds_read_b128 v[96:99], v1 offset:16
	ds_read_b128 v[100:103], v1 offset:32
	ds_read_b128 v[104:107], v1 offset:48
	v_xor_b32_e32 v2, 1, v227
	s_waitcnt lgkmcnt(3)
	v_mul_f32_e32 v1, v93, v93
	v_fmac_f32_e32 v1, v92, v92
	v_fmac_f32_e32 v1, v94, v94
	v_fmac_f32_e32 v1, v95, v95
	s_waitcnt lgkmcnt(2)
	v_fmac_f32_e32 v1, v96, v96
	v_fmac_f32_e32 v1, v97, v97
	v_fmac_f32_e32 v1, v98, v98
	v_fmac_f32_e32 v1, v99, v99
	s_waitcnt lgkmcnt(1)
	v_pk_mul_f32 v[110:111], v[100:101], v[100:101]
	v_pk_mul_f32 v[108:109], v[102:103], v[102:103]
	v_add_f32_e32 v1, v110, v1
	v_add_f32_e32 v1, v111, v1
	v_add_f32_e32 v1, v108, v1
	v_add_f32_e32 v1, v109, v1
	s_waitcnt lgkmcnt(0)
	v_pk_mul_f32 v[110:111], v[104:105], v[104:105]
	v_pk_mul_f32 v[108:109], v[106:107], v[106:107]
	v_add_f32_e32 v1, v110, v1
	v_add_f32_e32 v1, v111, v1
	v_add_f32_e32 v1, v108, v1
	v_and_b32_e32 v108, 64, v227
	v_add_u32_e32 v108, 64, v108
	v_cmp_lt_i32_e32 vcc, v2, v108
	v_add_f32_e32 v1, v109, v1
	v_and_b32_e32 v109, 0xffff0000, v56
	v_cndmask_b32_e32 v2, v227, v2, vcc
	v_lshlrev_b32_e32 v2, 2, v2
	ds_bpermute_b32 v2, v2, v1
	v_mov_b32_e32 v133, v3
	s_waitcnt lgkmcnt(0)
	v_add_f32_e32 v1, v1, v2
	v_xor_b32_e32 v2, 2, v227
	v_cmp_lt_i32_e32 vcc, v2, v108
	s_nop 1
	v_cndmask_b32_e32 v2, v227, v2, vcc
	v_lshlrev_b32_e32 v2, 2, v2
	ds_bpermute_b32 v2, v2, v1
	s_waitcnt lgkmcnt(0)
	v_add_f32_e32 v1, v1, v2
	v_xor_b32_e32 v2, 4, v227
	v_cmp_lt_i32_e32 vcc, v2, v108
	v_lshlrev_b32_e32 v108, 16, v56
	v_mul_f32_e32 v56, 0xbfb8aa3b, v109
	v_cndmask_b32_e32 v2, v227, v2, vcc
	v_lshlrev_b32_e32 v2, 2, v2
	ds_bpermute_b32 v2, v2, v1
	v_exp_f32_e32 v56, v56
	s_waitcnt lgkmcnt(0)
	v_add_f32_e32 v1, v1, v2
	v_fmamk_f32 v1, v1, 0x3c000000, v223
	v_mul_f32_e32 v2, 0x4b800000, v1
	v_cmp_gt_f32_e32 vcc, s97, v1
	s_nop 1
	v_cndmask_b32_e32 v1, v1, v2, vcc
	v_rsq_f32_e32 v1, v1
	s_nop 0
	v_mul_f32_e32 v2, 0x45800000, v1
	v_cndmask_b32_e32 v2, v1, v2, vcc
	v_mul_f32_e32 v1, 0xbfb8aa3b, v108
	v_exp_f32_e32 v1, v1
	v_pk_mul_f32 v[92:93], v[92:93], v[2:3] op_sel_hi:[1,0]
	v_pk_mul_f32 v[100:101], v[100:101], v[2:3] op_sel_hi:[1,0]
	v_pk_mul_f32 v[94:95], v[94:95], v[2:3] op_sel_hi:[1,0]
	v_add_f32_e32 v1, 1.0, v1
	v_rcp_f32_e32 v110, v1
	v_add_f32_e32 v1, 1.0, v56
	v_mul_f32_e32 v56, 0xbfb8aa3b, v113
	v_exp_f32_e32 v56, v56
	v_rcp_f32_e32 v111, v1
	v_add_f32_e32 v1, 1.0, v52
	v_rcp_f32_e32 v114, v1
	v_add_f32_e32 v1, 1.0, v56
	v_rcp_f32_e32 v115, v1
	v_lshlrev_b32_e32 v56, 16, v57
	v_pk_mul_f32 v[108:109], v[110:111], v[108:109]
	v_mul_f32_e32 v1, 0xbfb8aa3b, v56
	v_and_b32_e32 v57, 0xffff0000, v57
	v_pk_mul_f32 v[92:93], v[108:109], v[92:93]
	v_pk_mul_f32 v[108:109], v[114:115], v[112:113]
	v_exp_f32_e32 v1, v1
	v_mul_f32_e32 v52, 0xbfb8aa3b, v57
	v_pk_mul_f32 v[100:101], v[108:109], v[100:101]
	v_exp_f32_e32 v108, v52
	v_add_f32_e32 v1, 1.0, v1
	v_rcp_f32_e32 v52, v1
	v_and_b32_e32 v109, 0xffff0000, v53
	v_add_f32_e32 v1, 1.0, v108
	v_lshlrev_b32_e32 v108, 16, v53
	v_mul_f32_e32 v53, 0xbfb8aa3b, v108
	v_exp_f32_e32 v110, v53
	v_mul_f32_e32 v53, 0xbfb8aa3b, v109
	v_exp_f32_e32 v111, v53
	v_rcp_f32_e32 v53, v1
	v_add_f32_e32 v1, 1.0, v110
	v_rcp_f32_e32 v110, v1
	v_add_f32_e32 v1, 1.0, v111
	v_rcp_f32_e32 v111, v1
	v_pk_mul_f32 v[52:53], v[52:53], v[56:57]
	v_pk_mul_f32 v[96:97], v[96:97], v[2:3] op_sel_hi:[1,0]
	v_pk_mul_f32 v[56:57], v[52:53], v[94:95]
	v_pk_mul_f32 v[52:53], v[102:103], v[2:3] op_sel_hi:[1,0]
	v_pk_mul_f32 v[94:95], v[110:111], v[108:109]
	v_lshlrev_b32_e32 v108, 16, v54
	v_pk_mul_f32 v[94:95], v[94:95], v[52:53]
	v_lshlrev_b32_e32 v52, 16, v58
	v_mul_f32_e32 v1, 0xbfb8aa3b, v52
	v_and_b32_e32 v53, 0xffff0000, v58
	v_exp_f32_e32 v1, v1
	v_mul_f32_e32 v58, 0xbfb8aa3b, v53
	v_exp_f32_e32 v58, v58
	v_and_b32_e32 v109, 0xffff0000, v54
	v_add_f32_e32 v1, 1.0, v1
	v_mul_f32_e32 v54, 0xbfb8aa3b, v108
	v_rcp_f32_e32 v102, v1
	v_add_f32_e32 v1, 1.0, v58
	v_exp_f32_e32 v54, v54
	v_mul_f32_e32 v58, 0xbfb8aa3b, v109
	v_exp_f32_e32 v58, v58
	v_rcp_f32_e32 v103, v1
	v_add_f32_e32 v1, 1.0, v54
	v_rcp_f32_e32 v110, v1
	v_add_f32_e32 v1, 1.0, v58
	v_rcp_f32_e32 v111, v1
	v_pk_mul_f32 v[52:53], v[102:103], v[52:53]
	v_pk_mul_f32 v[102:103], v[110:111], v[108:109]
	v_pk_mul_f32 v[96:97], v[52:53], v[96:97]
	v_pk_mul_f32 v[52:53], v[104:105], v[2:3] op_sel_hi:[1,0]
	s_nop 0
	v_pk_mul_f32 v[102:103], v[102:103], v[52:53]
	v_lshlrev_b32_e32 v52, 16, v59
	v_mul_f32_e32 v1, 0xbfb8aa3b, v52
	v_and_b32_e32 v53, 0xffff0000, v59
	v_exp_f32_e32 v1, v1
	v_mul_f32_e32 v54, 0xbfb8aa3b, v53
	v_exp_f32_e32 v104, v54
	v_pk_mul_f32 v[58:59], v[98:99], v[2:3] op_sel_hi:[1,0]
	v_lshlrev_b32_e32 v98, 16, v55
	v_add_f32_e32 v1, 1.0, v1
	v_and_b32_e32 v99, 0xffff0000, v55
	v_mul_f32_e32 v55, 0xbfb8aa3b, v98
	v_rcp_f32_e32 v54, v1
	v_add_f32_e32 v1, 1.0, v104
	v_exp_f32_e32 v104, v55
	v_mul_f32_e32 v55, 0xbfb8aa3b, v99
	v_exp_f32_e32 v105, v55
	v_rcp_f32_e32 v55, v1
	v_add_f32_e32 v1, 1.0, v104
	v_rcp_f32_e32 v104, v1
	v_add_f32_e32 v1, 1.0, v105
	v_rcp_f32_e32 v105, v1
	v_pk_mul_f32 v[52:53], v[54:55], v[52:53]
	v_pk_mul_f32 v[54:55], v[104:105], v[98:99]
	v_pk_mul_f32 v[58:59], v[52:53], v[58:59]
	v_pk_mul_f32 v[52:53], v[106:107], v[2:3] op_sel_hi:[1,0]
	s_nop 0
	v_pk_mul_f32 v[98:99], v[54:55], v[52:53]
	v_cvt_pk_bf16_f32 v53, v56, v57
	v_add_u32_e32 v56, s28, v134
	v_ashrrev_i32_e32 v57, 31, v56
	v_lshlrev_b64 v[56:57], 12, v[56:57]
	v_lshl_add_u64 v[56:57], s[82:83], 0, v[56:57]
	v_lshl_add_u64 v[56:57], v[56:57], 0, s[52:53]
	v_lshl_add_u64 v[56:57], v[56:57], 0, v[132:133]
	v_cvt_pk_bf16_f32 v55, v58, v59
	v_lshl_add_u64 v[58:59], v[56:57], 0, s[4:5]
	s_mov_b32 s4, 0x43cae000
	v_add_co_u32_e32 v56, vcc, s4, v56
	v_cvt_pk_bf16_f32 v52, v92, v93
	v_cvt_pk_bf16_f32 v54, v96, v97
	v_addc_co_u32_e32 v57, vcc, 0, v57, vcc
	global_store_dwordx4 v[56:57], v[52:55], off offset:3072
	s_mov_b64 s[28:29], -1
	s_and_b64 vcc, s[44:45], exec
	v_cvt_pk_bf16_f32 v52, v100, v101
	v_cvt_pk_bf16_f32 v53, v94, v95
	v_cvt_pk_bf16_f32 v54, v102, v103
	v_cvt_pk_bf16_f32 v55, v98, v99
	global_store_dwordx4 v[58:59], v[52:55], off offset:16
	s_barrier
	s_cbranch_vccz .LBB0_770
	s_ashr_i32 s16, s25, 12
	s_lshl_b64 s[4:5], s[42:43], 23
	s_add_u32 s17, s37, s4
	s_addc_u32 s25, s78, s5
	s_lshl_b32 s4, s7, 8
	s_lshl_b32 s5, s16, 7
	s_add_i32 s4, s4, s5
	s_ashr_i32 s5, s4, 31
	s_lshl_b64 s[4:5], s[4:5], 11
	s_add_u32 s16, s17, s4
	s_addc_u32 s17, s25, s5
	s_mov_b64 s[28:29], 0
